# speedup vs baseline: 1.0027x; 1.0027x over previous
.Lgu_skipzero:
.LBB8_12:
	ds_read_b128 v[146:149], v188
	ds_read_b128 v[150:153], v188 offset:1024
	ds_read_b128 v[154:157], v188 offset:2048
	ds_read_b128 v[158:161], v188 offset:3072
	ds_read_b128 v[226:229], v190
	ds_read_b128 v[230:233], v190 offset:1024
	ds_read_b128 v[234:237], v190 offset:2048
	ds_read_b128 v[238:241], v190 offset:3072
	s_cmp_eq_u32 s51, s61
	s_cselect_b64 s[66:67], -1, 0
	s_add_i32 s61, s61, 2
	s_and_b64 s[34:35], s[66:67], exec
	s_cselect_b32 s35, s31, s60
	s_cselect_b32 s34, s30, s59
	s_cselect_b32 s64, s37, s57
	s_lshl_b32 s65, s64, 13
	s_and_b64 s[66:67], s[66:67], exec
	s_cselect_b32 s63, 0, s62
	s_add_i32 s68, s65, s63
	ds_read_b128 v[194:197], v189
	ds_read_b128 v[198:201], v189 offset:1024
	ds_read_b128 v[202:205], v189 offset:2048
	ds_read_b128 v[206:209], v189 offset:3072
	ds_read_b128 v[210:213], v189 offset:4096
	ds_read_b128 v[214:217], v189 offset:5120
	ds_read_b128 v[218:221], v189 offset:6144
	ds_read_b128 v[222:225], v189 offset:7168
	s_ashr_i32 s69, s68, 31
	s_waitcnt vmcnt(0)
	s_lshl_b64 s[66:67], s[68:69], 1
	v_pk_add_f16 v14, v14, v10
	v_pk_add_f16 v15, v15, v11
	v_pk_add_f16 v16, v16, v12
	v_pk_add_f16 v17, v17, v13
	s_add_u32 s70, s8, s66
	v_pk_max_f16 v17, v17, 0
	v_pk_max_f16 v16, v16, 0
	v_pk_max_f16 v15, v15, 0
	v_pk_max_f16 v14, v14, 0
	v_pk_add_f16 v6, v6, v10
	v_pk_add_f16 v7, v7, v11
	v_pk_add_f16 v8, v8, v12
	v_pk_add_f16 v9, v9, v13
	s_addc_u32 s71, s9, s67
	s_add_i32 s68, s68, s65
	v_pk_max_f16 v9, v9, 0
	v_pk_max_f16 v8, v8, 0
	v_pk_max_f16 v7, v7, 0
	v_pk_max_f16 v6, v6, 0
	ds_write_b128 v186, v[14:17] offset:49152
	ds_write_b128 v186, v[6:9] offset:57344
	s_ashr_i32 s69, s68, 31
	s_lshl_b32 s66, s64, 14
	s_lshl_b64 s[68:69], s[68:69], 1
	global_load_dwordx4 v[6:9], v184, s[70:71]
	s_add_u32 s68, s10, s68
	global_load_dwordx4 v[10:13], v185, s[70:71]
	s_addc_u32 s69, s11, s69
	global_load_dwordx4 v[14:17], v183, s[68:69]
	s_waitcnt lgkmcnt(2)
	s_barrier
	s_waitcnt lgkmcnt(0)
	s_setprio 1
	s_waitcnt lgkmcnt(0)
	v_mfma_f32_16x16x32_f16 v[138:141], v[146:149], v[194:197], v[138:141]
	v_mfma_f32_16x16x32_f16 v[142:145], v[154:157], v[194:197], v[142:145]
	v_mfma_f32_16x16x32_f16 v[126:129], v[146:149], v[202:205], v[126:129]
	v_mfma_f32_16x16x32_f16 v[122:125], v[154:157], v[202:205], v[122:125]
	v_mfma_f32_16x16x32_f16 v[110:113], v[146:149], v[210:213], v[110:113]
	v_mfma_f32_16x16x32_f16 v[106:109], v[154:157], v[210:213], v[106:109]
	v_mfma_f32_16x16x32_f16 v[94:97], v[146:149], v[218:221], v[94:97]
	v_mfma_f32_16x16x32_f16 v[90:93], v[154:157], v[218:221], v[90:93]
	v_mfma_f32_16x16x32_f16 v[138:141], v[150:153], v[198:201], v[138:141]
	v_mfma_f32_16x16x32_f16 v[142:145], v[158:161], v[198:201], v[142:145]
	v_mfma_f32_16x16x32_f16 v[126:129], v[150:153], v[206:209], v[126:129]
	v_mfma_f32_16x16x32_f16 v[122:125], v[158:161], v[206:209], v[122:125]
	v_mfma_f32_16x16x32_f16 v[110:113], v[150:153], v[214:217], v[110:113]
	v_mfma_f32_16x16x32_f16 v[106:109], v[158:161], v[214:217], v[106:109]
	v_mfma_f32_16x16x32_f16 v[94:97], v[150:153], v[222:225], v[94:97]
	v_mfma_f32_16x16x32_f16 v[90:93], v[158:161], v[222:225], v[90:93]
	s_setprio 0
	s_waitcnt lgkmcnt(0)
	s_setprio 1
	s_waitcnt lgkmcnt(0)
	v_mfma_f32_16x16x32_f16 v[134:137], v[226:229], v[194:197], v[134:137]
	v_mfma_f32_16x16x32_f16 v[130:133], v[234:237], v[194:197], v[130:133]
	v_mfma_f32_16x16x32_f16 v[118:121], v[226:229], v[202:205], v[118:121]
	v_mfma_f32_16x16x32_f16 v[114:117], v[234:237], v[202:205], v[114:117]
	v_mfma_f32_16x16x32_f16 v[102:105], v[226:229], v[210:213], v[102:105]
	v_mfma_f32_16x16x32_f16 v[98:101], v[234:237], v[210:213], v[98:101]
	v_mfma_f32_16x16x32_f16 v[86:89], v[226:229], v[218:221], v[86:89]
	v_mfma_f32_16x16x32_f16 v[82:85], v[234:237], v[218:221], v[82:85]
	v_mfma_f32_16x16x32_f16 v[134:137], v[230:233], v[198:201], v[134:137]
	v_mfma_f32_16x16x32_f16 v[130:133], v[238:241], v[198:201], v[130:133]
	v_mfma_f32_16x16x32_f16 v[118:121], v[230:233], v[206:209], v[118:121]
	v_mfma_f32_16x16x32_f16 v[114:117], v[238:241], v[206:209], v[114:117]
	v_mfma_f32_16x16x32_f16 v[102:105], v[230:233], v[214:217], v[102:105]
	v_mfma_f32_16x16x32_f16 v[98:101], v[238:241], v[214:217], v[98:101]
	v_mfma_f32_16x16x32_f16 v[86:89], v[230:233], v[222:225], v[86:89]
	v_mfma_f32_16x16x32_f16 v[82:85], v[238:241], v[222:225], v[82:85]
	s_setprio 0
	s_or_b32 s64, s65, 0x1000
	s_add_i32 s68, s64, s63
	s_barrier
	s_add_i32 s81, s53, s45
	v_lshl_add_u64 v[170:171], s[34:35], 0, v[162:163]
	s_mov_b32 m0, s81
	global_load_lds_dwordx4 v[170:171], off
	v_lshl_add_u64 v[242:243], s[34:35], 0, v[164:165]
	s_add_i32 m0, s81, 0x2000
	s_nop 0
	global_load_lds_dwordx4 v[242:243], off
	s_add_u32 s34, s34, s22
	s_addc_u32 s35, s35, s23
	s_add_i32 s82, s54, s45
	v_lshl_add_u64 v[244:245], s[34:35], 0, v[162:163]
	s_mov_b32 m0, s82
	v_lshl_add_u64 v[246:247], s[34:35], 0, v[164:165]
	global_load_lds_dwordx4 v[244:245], off
	s_add_i32 m0, s82, 0x2000
	s_nop 0
	global_load_lds_dwordx4 v[246:247], off
	ds_read_b128 v[194:197], v189 offset:16384
	ds_read_b128 v[198:201], v189 offset:17408
	ds_read_b128 v[202:205], v189 offset:18432
	ds_read_b128 v[206:209], v189 offset:19456
	ds_read_b128 v[210:213], v189 offset:20480
	ds_read_b128 v[214:217], v189 offset:21504
	ds_read_b128 v[218:221], v189 offset:22528
	ds_read_b128 v[222:225], v189 offset:23552
	s_ashr_i32 s69, s68, 31
	s_lshl_b64 s[68:69], s[68:69], 1
	s_waitcnt vmcnt(4)
	s_add_u32 s68, s8, s68
	v_pk_add_f16 v6, v6, v14
	v_pk_add_f16 v7, v7, v15
	v_pk_add_f16 v8, v8, v16
	v_pk_add_f16 v9, v9, v17
	s_addc_u32 s69, s9, s69
	s_or_b32 s67, s66, 0x2000
	v_pk_max_f16 v9, v9, 0
	v_pk_max_f16 v8, v8, 0
	v_pk_max_f16 v7, v7, 0
	v_pk_max_f16 v6, v6, 0
	v_pk_add_f16 v10, v10, v14
	v_pk_add_f16 v11, v11, v15
	v_pk_add_f16 v12, v12, v16
	v_pk_add_f16 v13, v13, v17
	s_add_i32 s70, s67, s63
	v_pk_max_f16 v13, v13, 0
	v_pk_max_f16 v12, v12, 0
	v_pk_max_f16 v11, v11, 0
	v_pk_max_f16 v10, v10, 0
	ds_write_b128 v186, v[6:9]
	ds_write_b128 v186, v[10:13] offset:8192
	s_ashr_i32 s71, s70, 31
	s_lshl_b64 s[70:71], s[70:71], 1
	global_load_dwordx4 v[6:9], v184, s[68:69]
	s_add_u32 s70, s10, s70
	global_load_dwordx4 v[10:13], v185, s[68:69]
	s_addc_u32 s71, s11, s71
	global_load_dwordx4 v[14:17], v183, s[70:71]
	s_waitcnt lgkmcnt(2)
	s_barrier
	s_waitcnt lgkmcnt(0)
	s_setprio 1
	s_waitcnt lgkmcnt(0)
	v_mfma_f32_16x16x32_f16 v[78:81], v[146:149], v[194:197], v[78:81]
	v_mfma_f32_16x16x32_f16 v[74:77], v[154:157], v[194:197], v[74:77]
	v_mfma_f32_16x16x32_f16 v[62:65], v[146:149], v[202:205], v[62:65]
	v_mfma_f32_16x16x32_f16 v[58:61], v[154:157], v[202:205], v[58:61]
	v_mfma_f32_16x16x32_f16 v[46:49], v[146:149], v[210:213], v[46:49]
	v_mfma_f32_16x16x32_f16 v[42:45], v[154:157], v[210:213], v[42:45]
	v_mfma_f32_16x16x32_f16 v[30:33], v[146:149], v[218:221], v[30:33]
	v_mfma_f32_16x16x32_f16 v[26:29], v[154:157], v[218:221], v[26:29]
	v_mfma_f32_16x16x32_f16 v[78:81], v[150:153], v[198:201], v[78:81]
	v_mfma_f32_16x16x32_f16 v[74:77], v[158:161], v[198:201], v[74:77]
	v_mfma_f32_16x16x32_f16 v[62:65], v[150:153], v[206:209], v[62:65]
	v_mfma_f32_16x16x32_f16 v[58:61], v[158:161], v[206:209], v[58:61]
	v_mfma_f32_16x16x32_f16 v[46:49], v[150:153], v[214:217], v[46:49]
	v_mfma_f32_16x16x32_f16 v[42:45], v[158:161], v[214:217], v[42:45]
	v_mfma_f32_16x16x32_f16 v[30:33], v[150:153], v[222:225], v[30:33]
	v_mfma_f32_16x16x32_f16 v[26:29], v[158:161], v[222:225], v[26:29]
	s_setprio 0
	s_setprio 1
	v_mfma_f32_16x16x32_f16 v[70:73], v[226:229], v[194:197], v[70:73]
	v_mfma_f32_16x16x32_f16 v[66:69], v[234:237], v[194:197], v[66:69]
	v_mfma_f32_16x16x32_f16 v[54:57], v[226:229], v[202:205], v[54:57]
	v_mfma_f32_16x16x32_f16 v[50:53], v[234:237], v[202:205], v[50:53]
	v_mfma_f32_16x16x32_f16 v[38:41], v[226:229], v[210:213], v[38:41]
	v_mfma_f32_16x16x32_f16 v[34:37], v[234:237], v[210:213], v[34:37]
	v_mfma_f32_16x16x32_f16 v[22:25], v[226:229], v[218:221], v[22:25]
	v_mfma_f32_16x16x32_f16 v[18:21], v[234:237], v[218:221], v[18:21]
	v_mfma_f32_16x16x32_f16 v[70:73], v[230:233], v[198:201], v[70:73]
	v_mfma_f32_16x16x32_f16 v[66:69], v[238:241], v[198:201], v[66:69]
	v_mfma_f32_16x16x32_f16 v[54:57], v[230:233], v[206:209], v[54:57]
	v_mfma_f32_16x16x32_f16 v[50:53], v[238:241], v[206:209], v[50:53]
	v_mfma_f32_16x16x32_f16 v[38:41], v[230:233], v[214:217], v[38:41]
	v_mfma_f32_16x16x32_f16 v[34:37], v[238:241], v[214:217], v[34:37]
	v_mfma_f32_16x16x32_f16 v[22:25], v[230:233], v[222:225], v[22:25]
	v_mfma_f32_16x16x32_f16 v[18:21], v[238:241], v[222:225], v[18:21]
	s_setprio 0
	s_barrier
	ds_read_b128 v[146:149], v191
	ds_read_b128 v[150:153], v191 offset:1024
	ds_read_b128 v[154:157], v191 offset:2048
	ds_read_b128 v[158:161], v191 offset:3072
	ds_read_b128 v[226:229], v192
	ds_read_b128 v[230:233], v192 offset:1024
	ds_read_b128 v[234:237], v192 offset:2048
	ds_read_b128 v[238:241], v192 offset:3072
	s_or_b32 s70, s63, 64
	s_ashr_i32 s35, s65, 31
	s_ashr_i32 s69, s63, 31
	s_add_u32 s34, s63, s65
	s_addc_u32 s35, s69, s35
	s_lshl_b64 s[34:35], s[34:35], 1
	s_add_u32 s34, s8, s34
	s_addc_u32 s35, s9, s35
	s_add_u32 s34, s34, 0x80
	ds_read_b128 v[194:197], v189 offset:32768
	ds_read_b128 v[198:201], v189 offset:33792
	ds_read_b128 v[202:205], v189 offset:34816
	ds_read_b128 v[206:209], v189 offset:35840
	ds_read_b128 v[210:213], v189 offset:36864
	ds_read_b128 v[214:217], v189 offset:37888
	ds_read_b128 v[218:221], v189 offset:38912
	ds_read_b128 v[222:225], v189 offset:39936
	s_addc_u32 s35, s35, 0
	s_ashr_i32 s65, s66, 31
	s_waitcnt vmcnt(0)
	s_add_u32 s68, s63, s66
	v_pk_add_f16 v6, v6, v14
	v_pk_add_f16 v7, v7, v15
	v_pk_add_f16 v8, v8, v16
	v_pk_add_f16 v9, v9, v17
	s_addc_u32 s69, s69, s65
	v_pk_max_f16 v9, v9, 0
	v_pk_max_f16 v8, v8, 0
	v_pk_max_f16 v7, v7, 0
	v_pk_max_f16 v6, v6, 0
	v_pk_add_f16 v10, v10, v14
	v_pk_add_f16 v11, v11, v15
	v_pk_add_f16 v12, v12, v16
	v_pk_add_f16 v13, v13, v17
	s_lshl_b64 s[68:69], s[68:69], 1
	v_pk_max_f16 v13, v13, 0
	v_pk_max_f16 v12, v12, 0
	v_pk_max_f16 v11, v11, 0
	v_pk_max_f16 v10, v10, 0
	ds_write_b128 v186, v[6:9] offset:16384
	ds_write_b128 v186, v[10:13] offset:24576
	s_add_u32 s63, s10, s68
	s_addc_u32 s65, s11, s69
	global_load_dwordx4 v[6:9], v184, s[34:35]
	s_add_u32 s68, s63, 0x80
	global_load_dwordx4 v[10:13], v185, s[34:35]
	s_addc_u32 s69, s65, 0
	global_load_dwordx4 v[14:17], v183, s[68:69]
	s_waitcnt lgkmcnt(2)
	s_barrier
	s_waitcnt lgkmcnt(0)
	s_setprio 1
	s_waitcnt lgkmcnt(0)
	v_mfma_f32_16x16x32_f16 v[138:141], v[146:149], v[194:197], v[138:141]
	v_mfma_f32_16x16x32_f16 v[142:145], v[154:157], v[194:197], v[142:145]
	v_mfma_f32_16x16x32_f16 v[126:129], v[146:149], v[202:205], v[126:129]
	v_mfma_f32_16x16x32_f16 v[122:125], v[154:157], v[202:205], v[122:125]
	v_mfma_f32_16x16x32_f16 v[110:113], v[146:149], v[210:213], v[110:113]
	v_mfma_f32_16x16x32_f16 v[106:109], v[154:157], v[210:213], v[106:109]
	v_mfma_f32_16x16x32_f16 v[94:97], v[146:149], v[218:221], v[94:97]
	v_mfma_f32_16x16x32_f16 v[90:93], v[154:157], v[218:221], v[90:93]
	v_mfma_f32_16x16x32_f16 v[138:141], v[150:153], v[198:201], v[138:141]
	v_mfma_f32_16x16x32_f16 v[142:145], v[158:161], v[198:201], v[142:145]
	v_mfma_f32_16x16x32_f16 v[126:129], v[150:153], v[206:209], v[126:129]
	v_mfma_f32_16x16x32_f16 v[122:125], v[158:161], v[206:209], v[122:125]
	v_mfma_f32_16x16x32_f16 v[110:113], v[150:153], v[214:217], v[110:113]
	v_mfma_f32_16x16x32_f16 v[106:109], v[158:161], v[214:217], v[106:109]
	v_mfma_f32_16x16x32_f16 v[94:97], v[150:153], v[222:225], v[94:97]
	v_mfma_f32_16x16x32_f16 v[90:93], v[158:161], v[222:225], v[90:93]
	s_setprio 0
	s_waitcnt lgkmcnt(0)
	s_setprio 1
	s_waitcnt lgkmcnt(0)
	v_mfma_f32_16x16x32_f16 v[134:137], v[226:229], v[194:197], v[134:137]
	v_mfma_f32_16x16x32_f16 v[130:133], v[234:237], v[194:197], v[130:133]
	v_mfma_f32_16x16x32_f16 v[118:121], v[226:229], v[202:205], v[118:121]
	v_mfma_f32_16x16x32_f16 v[114:117], v[234:237], v[202:205], v[114:117]
	v_mfma_f32_16x16x32_f16 v[102:105], v[226:229], v[210:213], v[102:105]
	v_mfma_f32_16x16x32_f16 v[98:101], v[234:237], v[210:213], v[98:101]
	v_mfma_f32_16x16x32_f16 v[86:89], v[226:229], v[218:221], v[86:89]
	v_mfma_f32_16x16x32_f16 v[82:85], v[234:237], v[218:221], v[82:85]
	v_mfma_f32_16x16x32_f16 v[134:137], v[230:233], v[198:201], v[134:137]
	v_mfma_f32_16x16x32_f16 v[130:133], v[238:241], v[198:201], v[130:133]
	v_mfma_f32_16x16x32_f16 v[118:121], v[230:233], v[206:209], v[118:121]
	v_mfma_f32_16x16x32_f16 v[114:117], v[238:241], v[206:209], v[114:117]
	v_mfma_f32_16x16x32_f16 v[102:105], v[230:233], v[214:217], v[102:105]
	v_mfma_f32_16x16x32_f16 v[98:101], v[238:241], v[214:217], v[98:101]
	v_mfma_f32_16x16x32_f16 v[86:89], v[230:233], v[222:225], v[86:89]
	v_mfma_f32_16x16x32_f16 v[82:85], v[238:241], v[222:225], v[82:85]
	s_setprio 0
	s_barrier
	s_add_i32 s81, s55, s45
	v_lshl_add_u64 v[170:171], v[170:171], 0, s[26:27]
	s_mov_b32 m0, s81
	global_load_lds_dwordx4 v[170:171], off
	v_lshl_add_u64 v[170:171], v[242:243], 0, s[26:27]
	s_add_i32 m0, s81, 0x2000
	s_nop 0
	global_load_lds_dwordx4 v[170:171], off
	s_add_i32 s82, s56, s45
	v_lshl_add_u64 v[248:249], v[244:245], 0, s[26:27]
	s_mov_b32 m0, s82
	s_nop 0
	global_load_lds_dwordx4 v[248:249], off
	v_lshl_add_u64 v[248:249], v[246:247], 0, s[26:27]
	s_add_i32 m0, s82, 0x2000
	s_nop 0
	global_load_lds_dwordx4 v[248:249], off
	ds_read_b128 v[194:197], v189 offset:49152
	ds_read_b128 v[198:201], v189 offset:50176
	ds_read_b128 v[202:205], v189 offset:51200
	ds_read_b128 v[206:209], v189 offset:52224
	ds_read_b128 v[210:213], v189 offset:53248
	ds_read_b128 v[214:217], v189 offset:54272
	ds_read_b128 v[218:221], v189 offset:55296
	ds_read_b128 v[222:225], v189 offset:56320
	s_add_i32 s34, s64, s70
	s_ashr_i32 s35, s34, 31
	s_waitcnt vmcnt(4)
	s_lshl_b64 s[34:35], s[34:35], 1
	v_pk_add_f16 v6, v6, v14
	v_pk_add_f16 v7, v7, v15
	v_pk_add_f16 v8, v8, v16
	v_pk_add_f16 v9, v9, v17
	s_add_u32 s34, s8, s34
	v_pk_max_f16 v9, v9, 0
	v_pk_max_f16 v8, v8, 0
	v_pk_max_f16 v7, v7, 0
	v_pk_max_f16 v6, v6, 0
	v_pk_add_f16 v10, v10, v14
	v_pk_add_f16 v11, v11, v15
	v_pk_add_f16 v12, v12, v16
	v_pk_add_f16 v13, v13, v17
	s_addc_u32 s35, s9, s35
	s_add_i32 s64, s67, s70
	v_pk_max_f16 v13, v13, 0
	v_pk_max_f16 v12, v12, 0
	v_pk_max_f16 v11, v11, 0
	v_pk_max_f16 v10, v10, 0
	ds_write_b128 v186, v[6:9] offset:32768
	ds_write_b128 v186, v[10:13] offset:40960
	s_ashr_i32 s65, s64, 31
	s_lshl_b64 s[64:65], s[64:65], 1
	global_load_dwordx4 v[14:17], v184, s[34:35]
	s_add_u32 s64, s10, s64
	global_load_dwordx4 v[6:9], v185, s[34:35]
	s_addc_u32 s65, s11, s65
	global_load_dwordx4 v[10:13], v183, s[64:65]
	s_waitcnt lgkmcnt(2)
	s_barrier
	s_waitcnt lgkmcnt(0)
	s_setprio 1
	s_waitcnt lgkmcnt(0)
	v_mfma_f32_16x16x32_f16 v[78:81], v[146:149], v[194:197], v[78:81]
	v_mfma_f32_16x16x32_f16 v[74:77], v[154:157], v[194:197], v[74:77]
	v_mfma_f32_16x16x32_f16 v[62:65], v[146:149], v[202:205], v[62:65]
	v_mfma_f32_16x16x32_f16 v[58:61], v[154:157], v[202:205], v[58:61]
	v_mfma_f32_16x16x32_f16 v[46:49], v[146:149], v[210:213], v[46:49]
	v_mfma_f32_16x16x32_f16 v[42:45], v[154:157], v[210:213], v[42:45]
	v_mfma_f32_16x16x32_f16 v[30:33], v[146:149], v[218:221], v[30:33]
	v_mfma_f32_16x16x32_f16 v[26:29], v[154:157], v[218:221], v[26:29]
	v_mfma_f32_16x16x32_f16 v[78:81], v[150:153], v[198:201], v[78:81]
	v_mfma_f32_16x16x32_f16 v[74:77], v[158:161], v[198:201], v[74:77]
	v_mfma_f32_16x16x32_f16 v[62:65], v[150:153], v[206:209], v[62:65]
	v_mfma_f32_16x16x32_f16 v[58:61], v[158:161], v[206:209], v[58:61]
	v_mfma_f32_16x16x32_f16 v[46:49], v[150:153], v[214:217], v[46:49]
	v_mfma_f32_16x16x32_f16 v[42:45], v[158:161], v[214:217], v[42:45]
	v_mfma_f32_16x16x32_f16 v[30:33], v[150:153], v[222:225], v[30:33]
	v_mfma_f32_16x16x32_f16 v[26:29], v[158:161], v[222:225], v[26:29]
	s_setprio 0
	s_setprio 1
	v_mfma_f32_16x16x32_f16 v[70:73], v[226:229], v[194:197], v[70:73]
	v_mfma_f32_16x16x32_f16 v[66:69], v[234:237], v[194:197], v[66:69]
	v_mfma_f32_16x16x32_f16 v[54:57], v[226:229], v[202:205], v[54:57]
	v_mfma_f32_16x16x32_f16 v[50:53], v[234:237], v[202:205], v[50:53]
	v_mfma_f32_16x16x32_f16 v[38:41], v[226:229], v[210:213], v[38:41]
	v_mfma_f32_16x16x32_f16 v[34:37], v[234:237], v[210:213], v[34:37]
	v_mfma_f32_16x16x32_f16 v[22:25], v[226:229], v[218:221], v[22:25]
	v_mfma_f32_16x16x32_f16 v[18:21], v[234:237], v[218:221], v[18:21]
	v_mfma_f32_16x16x32_f16 v[70:73], v[230:233], v[198:201], v[70:73]
	v_mfma_f32_16x16x32_f16 v[66:69], v[238:241], v[198:201], v[66:69]
	v_mfma_f32_16x16x32_f16 v[54:57], v[230:233], v[206:209], v[54:57]
	v_mfma_f32_16x16x32_f16 v[50:53], v[238:241], v[206:209], v[50:53]
	v_mfma_f32_16x16x32_f16 v[38:41], v[230:233], v[214:217], v[38:41]
	v_mfma_f32_16x16x32_f16 v[34:37], v[238:241], v[214:217], v[34:37]
	v_mfma_f32_16x16x32_f16 v[22:25], v[230:233], v[222:225], v[22:25]
	v_mfma_f32_16x16x32_f16 v[18:21], v[238:241], v[222:225], v[18:21]
	s_setprio 0
	s_addk_i32 s62, 0x80
	s_add_u32 s59, s59, 0x100
	s_addc_u32 s60, s60, 0
	s_cmp_ge_i32 s61, s49
	s_barrier
	s_cbranch_scc0 .LBB8_12
	s_branch .LBB8_20

.Lgt_skipzero:
.LBB8_37:
	ds_read_b128 v[144:147], v173
	ds_read_b128 v[148:151], v173 offset:1024
	ds_read_b128 v[152:155], v173 offset:2048
	ds_read_b128 v[156:159], v173 offset:3072
	ds_read_b128 v[212:215], v177
	ds_read_b128 v[216:219], v177 offset:1024
	ds_read_b128 v[220:223], v177 offset:2048
	ds_read_b128 v[224:227], v177 offset:3072
	s_cmp_eq_u32 s49, s61
	s_cselect_b64 s[24:25], -1, 0
	s_and_b64 s[24:25], s[24:25], exec
	s_cselect_b32 s35, s23, s60
	s_cselect_b32 s34, s22, s59
	s_cselect_b32 s30, 0, s61
	s_cselect_b32 s31, s56, s57
	s_lshl_b32 s24, s30, 6
	s_lshl_b32 s62, s31, 14
	s_and_b32 s68, s24, 0x180
	s_or_b32 s24, s68, s62
	s_ashr_i32 s25, s24, 31
	s_lshl_b64 s[26:27], s[24:25], 1
	s_add_u32 s28, s8, s26
	s_addc_u32 s29, s9, s27
	s_lshl_b32 s25, s31, 6
	s_lshr_b32 s26, s30, 3
	ds_read_b128 v[180:183], v174
	ds_read_b128 v[184:187], v174 offset:1024
	ds_read_b128 v[188:191], v174 offset:2048
	ds_read_b128 v[192:195], v174 offset:3072
	ds_read_b128 v[196:199], v174 offset:4096
	ds_read_b128 v[200:203], v174 offset:5120
	ds_read_b128 v[204:207], v174 offset:6144
	ds_read_b128 v[208:211], v174 offset:7168
	s_waitcnt vmcnt(0)
	s_add_i32 s25, s25, s26
	v_pk_add_f16 v8, v8, v12
	v_pk_add_f16 v9, v9, v13
	v_pk_add_f16 v10, v10, v14
	v_pk_add_f16 v11, v11, v15
	s_lshl_b32 s63, s25, 9
	v_pk_max_f16 v11, v11, 0
	v_pk_max_f16 v10, v10, 0
	v_pk_max_f16 v9, v9, 0
	v_pk_max_f16 v8, v8, 0
	v_pk_add_f16 v0, v0, v4
	v_pk_add_f16 v1, v1, v5
	v_pk_add_f16 v2, v2, v6
	v_pk_add_f16 v3, v3, v7
	s_or_b32 s26, s63, s68
	v_pk_max_f16 v3, v3, 0
	v_pk_max_f16 v2, v2, 0
	v_pk_max_f16 v1, v1, 0
	v_pk_max_f16 v0, v0, 0
	ds_write_b128 v175, v[8:11] offset:49152
	ds_write_b128 v175, v[0:3] offset:57344
	s_ashr_i32 s27, s26, 31
	s_lshl_b64 s[30:31], s[26:27], 1
	global_load_dwordx4 v[0:3], v168, s[28:29]
	s_add_u32 s30, s10, s30
	global_load_dwordx4 v[4:7], v170, s[28:29]
	s_addc_u32 s31, s11, s31
	global_load_dwordx4 v[8:11], v169, s[30:31]
	global_load_dwordx4 v[12:15], v171, s[30:31]
	s_waitcnt lgkmcnt(2)
	s_barrier
	s_waitcnt lgkmcnt(0)
	s_setprio 1
	s_waitcnt lgkmcnt(0)
	v_mfma_f32_16x16x32_f16 v[136:139], v[144:147], v[180:183], v[136:139]
	v_mfma_f32_16x16x32_f16 v[140:143], v[152:155], v[180:183], v[140:143]
	v_mfma_f32_16x16x32_f16 v[124:127], v[144:147], v[188:191], v[124:127]
	v_mfma_f32_16x16x32_f16 v[120:123], v[152:155], v[188:191], v[120:123]
	v_mfma_f32_16x16x32_f16 v[108:111], v[144:147], v[196:199], v[108:111]
	v_mfma_f32_16x16x32_f16 v[104:107], v[152:155], v[196:199], v[104:107]
	v_mfma_f32_16x16x32_f16 v[92:95], v[144:147], v[204:207], v[92:95]
	v_mfma_f32_16x16x32_f16 v[88:91], v[152:155], v[204:207], v[88:91]
	v_mfma_f32_16x16x32_f16 v[136:139], v[148:151], v[184:187], v[136:139]
	v_mfma_f32_16x16x32_f16 v[140:143], v[156:159], v[184:187], v[140:143]
	v_mfma_f32_16x16x32_f16 v[124:127], v[148:151], v[192:195], v[124:127]
	v_mfma_f32_16x16x32_f16 v[120:123], v[156:159], v[192:195], v[120:123]
	v_mfma_f32_16x16x32_f16 v[108:111], v[148:151], v[200:203], v[108:111]
	v_mfma_f32_16x16x32_f16 v[104:107], v[156:159], v[200:203], v[104:107]
	v_mfma_f32_16x16x32_f16 v[92:95], v[148:151], v[208:211], v[92:95]
	v_mfma_f32_16x16x32_f16 v[88:91], v[156:159], v[208:211], v[88:91]
	s_setprio 0
	s_waitcnt lgkmcnt(0)
	s_setprio 1
	s_waitcnt lgkmcnt(0)
	v_mfma_f32_16x16x32_f16 v[132:135], v[212:215], v[180:183], v[132:135]
	v_mfma_f32_16x16x32_f16 v[128:131], v[220:223], v[180:183], v[128:131]
	v_mfma_f32_16x16x32_f16 v[116:119], v[212:215], v[188:191], v[116:119]
	v_mfma_f32_16x16x32_f16 v[112:115], v[220:223], v[188:191], v[112:115]
	v_mfma_f32_16x16x32_f16 v[100:103], v[212:215], v[196:199], v[100:103]
	v_mfma_f32_16x16x32_f16 v[96:99], v[220:223], v[196:199], v[96:99]
	v_mfma_f32_16x16x32_f16 v[84:87], v[212:215], v[204:207], v[84:87]
	v_mfma_f32_16x16x32_f16 v[80:83], v[220:223], v[204:207], v[80:83]
	v_mfma_f32_16x16x32_f16 v[132:135], v[216:219], v[184:187], v[132:135]
	v_mfma_f32_16x16x32_f16 v[128:131], v[224:227], v[184:187], v[128:131]
	v_mfma_f32_16x16x32_f16 v[116:119], v[216:219], v[192:195], v[116:119]
	v_mfma_f32_16x16x32_f16 v[112:115], v[224:227], v[192:195], v[112:115]
	v_mfma_f32_16x16x32_f16 v[100:103], v[216:219], v[200:203], v[100:103]
	v_mfma_f32_16x16x32_f16 v[96:99], v[224:227], v[200:203], v[96:99]
	v_mfma_f32_16x16x32_f16 v[84:87], v[216:219], v[208:211], v[84:87]
	v_mfma_f32_16x16x32_f16 v[80:83], v[224:227], v[208:211], v[80:83]
	s_setprio 0
	s_or_b32 s64, s62, 0x2000
	s_or_b32 s28, s68, s64
	s_ashr_i32 s29, s28, 31
	s_barrier
	s_add_i32 s81, s51, s44
	v_lshl_add_u64 v[166:167], s[34:35], 0, v[160:161]
	s_mov_b32 m0, s81
	global_load_lds_dwordx4 v[166:167], off
	v_lshl_add_u64 v[228:229], s[34:35], 0, v[162:163]
	s_add_i32 m0, s81, 0x2000
	s_nop 0
	global_load_lds_dwordx4 v[228:229], off
	s_add_u32 s34, s34, s14
	s_addc_u32 s35, s35, s15
	s_add_i32 s82, s52, s44
	v_lshl_add_u64 v[230:231], s[34:35], 0, v[160:161]
	s_mov_b32 m0, s82
	v_lshl_add_u64 v[232:233], s[34:35], 0, v[162:163]
	global_load_lds_dwordx4 v[230:231], off
	s_add_i32 m0, s82, 0x2000
	s_nop 0
	global_load_lds_dwordx4 v[232:233], off
	ds_read_b128 v[180:183], v174 offset:16384
	ds_read_b128 v[184:187], v174 offset:17408
	ds_read_b128 v[188:191], v174 offset:18432
	ds_read_b128 v[192:195], v174 offset:19456
	ds_read_b128 v[196:199], v174 offset:20480
	ds_read_b128 v[200:203], v174 offset:21504
	ds_read_b128 v[204:207], v174 offset:22528
	ds_read_b128 v[208:211], v174 offset:23552
	s_lshl_b64 s[30:31], s[28:29], 1
	s_waitcnt vmcnt(4)
	s_add_u32 s66, s8, s30
	v_pk_add_f16 v0, v0, v8
	v_pk_add_f16 v1, v1, v9
	v_pk_add_f16 v2, v2, v10
	v_pk_add_f16 v3, v3, v11
	s_addc_u32 s67, s9, s31
	s_add_i32 s65, s63, 0x4000
	v_pk_max_f16 v3, v3, 0
	v_pk_max_f16 v2, v2, 0
	v_pk_max_f16 v1, v1, 0
	v_pk_max_f16 v0, v0, 0
	v_pk_add_f16 v4, v4, v12
	v_pk_add_f16 v5, v5, v13
	v_pk_add_f16 v6, v6, v14
	v_pk_add_f16 v7, v7, v15
	s_or_b32 s30, s65, s68
	v_pk_max_f16 v7, v7, 0
	v_pk_max_f16 v6, v6, 0
	v_pk_max_f16 v5, v5, 0
	v_pk_max_f16 v4, v4, 0
	ds_write_b128 v175, v[0:3]
	ds_write_b128 v175, v[4:7] offset:8192
	s_ashr_i32 s31, s30, 31
	s_lshl_b64 s[68:69], s[30:31], 1
	global_load_dwordx4 v[0:3], v168, s[66:67]
	s_add_u32 s68, s10, s68
	global_load_dwordx4 v[4:7], v170, s[66:67]
	s_addc_u32 s69, s11, s69
	global_load_dwordx4 v[8:11], v169, s[68:69]
	global_load_dwordx4 v[12:15], v171, s[68:69]
	s_waitcnt lgkmcnt(2)
	s_barrier
	s_waitcnt lgkmcnt(0)
	s_setprio 1
	s_waitcnt lgkmcnt(0)
	v_mfma_f32_16x16x32_f16 v[76:79], v[144:147], v[180:183], v[76:79]
	v_mfma_f32_16x16x32_f16 v[72:75], v[152:155], v[180:183], v[72:75]
	v_mfma_f32_16x16x32_f16 v[60:63], v[144:147], v[188:191], v[60:63]
	v_mfma_f32_16x16x32_f16 v[56:59], v[152:155], v[188:191], v[56:59]
	v_mfma_f32_16x16x32_f16 v[44:47], v[144:147], v[196:199], v[44:47]
	v_mfma_f32_16x16x32_f16 v[40:43], v[152:155], v[196:199], v[40:43]
	v_mfma_f32_16x16x32_f16 v[28:31], v[144:147], v[204:207], v[28:31]
	v_mfma_f32_16x16x32_f16 v[24:27], v[152:155], v[204:207], v[24:27]
	v_mfma_f32_16x16x32_f16 v[76:79], v[148:151], v[184:187], v[76:79]
	v_mfma_f32_16x16x32_f16 v[72:75], v[156:159], v[184:187], v[72:75]
	v_mfma_f32_16x16x32_f16 v[60:63], v[148:151], v[192:195], v[60:63]
	v_mfma_f32_16x16x32_f16 v[56:59], v[156:159], v[192:195], v[56:59]
	v_mfma_f32_16x16x32_f16 v[44:47], v[148:151], v[200:203], v[44:47]
	v_mfma_f32_16x16x32_f16 v[40:43], v[156:159], v[200:203], v[40:43]
	v_mfma_f32_16x16x32_f16 v[28:31], v[148:151], v[208:211], v[28:31]
	v_mfma_f32_16x16x32_f16 v[24:27], v[156:159], v[208:211], v[24:27]
	s_setprio 0
	s_setprio 1
	v_mfma_f32_16x16x32_f16 v[68:71], v[212:215], v[180:183], v[68:71]
	v_mfma_f32_16x16x32_f16 v[64:67], v[220:223], v[180:183], v[64:67]
	v_mfma_f32_16x16x32_f16 v[52:55], v[212:215], v[188:191], v[52:55]
	v_mfma_f32_16x16x32_f16 v[48:51], v[220:223], v[188:191], v[48:51]
	v_mfma_f32_16x16x32_f16 v[36:39], v[212:215], v[196:199], v[36:39]
	v_mfma_f32_16x16x32_f16 v[32:35], v[220:223], v[196:199], v[32:35]
	v_mfma_f32_16x16x32_f16 v[20:23], v[212:215], v[204:207], v[20:23]
	v_mfma_f32_16x16x32_f16 v[16:19], v[220:223], v[204:207], v[16:19]
	v_mfma_f32_16x16x32_f16 v[68:71], v[216:219], v[184:187], v[68:71]
	v_mfma_f32_16x16x32_f16 v[64:67], v[224:227], v[184:187], v[64:67]
	v_mfma_f32_16x16x32_f16 v[52:55], v[216:219], v[192:195], v[52:55]
	v_mfma_f32_16x16x32_f16 v[48:51], v[224:227], v[192:195], v[48:51]
	v_mfma_f32_16x16x32_f16 v[36:39], v[216:219], v[200:203], v[36:39]
	v_mfma_f32_16x16x32_f16 v[32:35], v[224:227], v[200:203], v[32:35]
	v_mfma_f32_16x16x32_f16 v[20:23], v[216:219], v[208:211], v[20:23]
	v_mfma_f32_16x16x32_f16 v[16:19], v[224:227], v[208:211], v[16:19]
	s_setprio 0
	s_barrier
	ds_read_b128 v[144:147], v178
	ds_read_b128 v[148:151], v178 offset:1024
	ds_read_b128 v[152:155], v178 offset:2048
	ds_read_b128 v[156:159], v178 offset:3072
	ds_read_b128 v[212:215], v179
	ds_read_b128 v[216:219], v179 offset:1024
	ds_read_b128 v[220:223], v179 offset:2048
	ds_read_b128 v[224:227], v179 offset:3072
	s_ashr_i32 s25, s62, 31
	s_lshl_b64 s[24:25], s[24:25], 1
	s_add_u32 s24, s8, s24
	s_addc_u32 s25, s9, s25
	ds_read_b128 v[180:183], v174 offset:32768
	ds_read_b128 v[184:187], v174 offset:33792
	ds_read_b128 v[188:191], v174 offset:34816
	ds_read_b128 v[192:195], v174 offset:35840
	ds_read_b128 v[196:199], v174 offset:36864
	ds_read_b128 v[200:203], v174 offset:37888
	ds_read_b128 v[204:207], v174 offset:38912
	ds_read_b128 v[208:211], v174 offset:39936
	s_waitcnt vmcnt(0)
	s_add_u32 s24, s24, 0x80
	v_pk_add_f16 v0, v0, v8
	v_pk_add_f16 v1, v1, v9
	v_pk_add_f16 v2, v2, v10
	v_pk_add_f16 v3, v3, v11
	s_addc_u32 s25, s25, 0
	s_ashr_i32 s27, s63, 31
	v_pk_max_f16 v3, v3, 0
	v_pk_max_f16 v2, v2, 0
	v_pk_max_f16 v1, v1, 0
	v_pk_max_f16 v0, v0, 0
	v_pk_add_f16 v4, v4, v12
	v_pk_add_f16 v5, v5, v13
	v_pk_add_f16 v6, v6, v14
	v_pk_add_f16 v7, v7, v15
	s_lshl_b64 s[26:27], s[26:27], 1
	v_pk_max_f16 v7, v7, 0
	v_pk_max_f16 v6, v6, 0
	v_pk_max_f16 v5, v5, 0
	v_pk_max_f16 v4, v4, 0
	ds_write_b128 v175, v[0:3] offset:16384
	ds_write_b128 v175, v[4:7] offset:24576
	s_add_u32 s26, s10, s26
	s_addc_u32 s27, s11, s27
	global_load_dwordx4 v[0:3], v168, s[24:25]
	s_add_u32 s26, s26, 0x80
	global_load_dwordx4 v[4:7], v170, s[24:25]
	s_addc_u32 s27, s27, 0
	global_load_dwordx4 v[8:11], v169, s[26:27]
	global_load_dwordx4 v[12:15], v171, s[26:27]
	s_waitcnt lgkmcnt(2)
	s_barrier
	s_waitcnt lgkmcnt(0)
	s_setprio 1
	s_waitcnt lgkmcnt(0)
	v_mfma_f32_16x16x32_f16 v[136:139], v[144:147], v[180:183], v[136:139]
	v_mfma_f32_16x16x32_f16 v[140:143], v[152:155], v[180:183], v[140:143]
	v_mfma_f32_16x16x32_f16 v[124:127], v[144:147], v[188:191], v[124:127]
	v_mfma_f32_16x16x32_f16 v[120:123], v[152:155], v[188:191], v[120:123]
	v_mfma_f32_16x16x32_f16 v[108:111], v[144:147], v[196:199], v[108:111]
	v_mfma_f32_16x16x32_f16 v[104:107], v[152:155], v[196:199], v[104:107]
	v_mfma_f32_16x16x32_f16 v[92:95], v[144:147], v[204:207], v[92:95]
	v_mfma_f32_16x16x32_f16 v[88:91], v[152:155], v[204:207], v[88:91]
	v_mfma_f32_16x16x32_f16 v[136:139], v[148:151], v[184:187], v[136:139]
	v_mfma_f32_16x16x32_f16 v[140:143], v[156:159], v[184:187], v[140:143]
	v_mfma_f32_16x16x32_f16 v[124:127], v[148:151], v[192:195], v[124:127]
	v_mfma_f32_16x16x32_f16 v[120:123], v[156:159], v[192:195], v[120:123]
	v_mfma_f32_16x16x32_f16 v[108:111], v[148:151], v[200:203], v[108:111]
	v_mfma_f32_16x16x32_f16 v[104:107], v[156:159], v[200:203], v[104:107]
	v_mfma_f32_16x16x32_f16 v[92:95], v[148:151], v[208:211], v[92:95]
	v_mfma_f32_16x16x32_f16 v[88:91], v[156:159], v[208:211], v[88:91]
	s_setprio 0
	s_waitcnt lgkmcnt(0)
	s_setprio 1
	s_waitcnt lgkmcnt(0)
	v_mfma_f32_16x16x32_f16 v[132:135], v[212:215], v[180:183], v[132:135]
	v_mfma_f32_16x16x32_f16 v[128:131], v[220:223], v[180:183], v[128:131]
	v_mfma_f32_16x16x32_f16 v[116:119], v[212:215], v[188:191], v[116:119]
	v_mfma_f32_16x16x32_f16 v[112:115], v[220:223], v[188:191], v[112:115]
	v_mfma_f32_16x16x32_f16 v[100:103], v[212:215], v[196:199], v[100:103]
	v_mfma_f32_16x16x32_f16 v[96:99], v[220:223], v[196:199], v[96:99]
	v_mfma_f32_16x16x32_f16 v[84:87], v[212:215], v[204:207], v[84:87]
	v_mfma_f32_16x16x32_f16 v[80:83], v[220:223], v[204:207], v[80:83]
	v_mfma_f32_16x16x32_f16 v[132:135], v[216:219], v[184:187], v[132:135]
	v_mfma_f32_16x16x32_f16 v[128:131], v[224:227], v[184:187], v[128:131]
	v_mfma_f32_16x16x32_f16 v[116:119], v[216:219], v[192:195], v[116:119]
	v_mfma_f32_16x16x32_f16 v[112:115], v[224:227], v[192:195], v[112:115]
	v_mfma_f32_16x16x32_f16 v[100:103], v[216:219], v[200:203], v[100:103]
	v_mfma_f32_16x16x32_f16 v[96:99], v[224:227], v[200:203], v[96:99]
	v_mfma_f32_16x16x32_f16 v[84:87], v[216:219], v[208:211], v[84:87]
	v_mfma_f32_16x16x32_f16 v[80:83], v[224:227], v[208:211], v[80:83]
	s_setprio 0
	s_ashr_i32 s29, s64, 31
	s_lshl_b64 s[24:25], s[28:29], 1
	s_add_u32 s24, s8, s24
	s_barrier
	s_add_i32 s81, s53, s44
	v_lshl_add_u64 v[166:167], v[166:167], 0, s[20:21]
	s_mov_b32 m0, s81
	global_load_lds_dwordx4 v[166:167], off
	v_lshl_add_u64 v[166:167], v[228:229], 0, s[20:21]
	s_add_i32 m0, s81, 0x2000
	s_nop 0
	global_load_lds_dwordx4 v[166:167], off
	s_add_i32 s82, s54, s44
	v_lshl_add_u64 v[248:249], v[230:231], 0, s[20:21]
	s_mov_b32 m0, s82
	s_nop 0
	global_load_lds_dwordx4 v[248:249], off
	v_lshl_add_u64 v[248:249], v[232:233], 0, s[20:21]
	s_add_i32 m0, s82, 0x2000
	s_nop 0
	global_load_lds_dwordx4 v[248:249], off
	ds_read_b128 v[180:183], v174 offset:49152
	ds_read_b128 v[184:187], v174 offset:50176
	ds_read_b128 v[188:191], v174 offset:51200
	ds_read_b128 v[192:195], v174 offset:52224
	ds_read_b128 v[196:199], v174 offset:53248
	ds_read_b128 v[200:203], v174 offset:54272
	ds_read_b128 v[204:207], v174 offset:55296
	ds_read_b128 v[208:211], v174 offset:56320
	s_addc_u32 s25, s9, s25
	s_waitcnt vmcnt(4)
	s_add_u32 s24, s24, 0x80
	v_pk_add_f16 v0, v0, v8
	v_pk_add_f16 v1, v1, v9
	v_pk_add_f16 v2, v2, v10
	v_pk_add_f16 v3, v3, v11
	s_addc_u32 s25, s25, 0
	s_ashr_i32 s31, s65, 31
	v_pk_max_f16 v3, v3, 0
	v_pk_max_f16 v2, v2, 0
	v_pk_max_f16 v1, v1, 0
	v_pk_max_f16 v0, v0, 0
	v_pk_add_f16 v4, v4, v12
	v_pk_add_f16 v5, v5, v13
	v_pk_add_f16 v6, v6, v14
	v_pk_add_f16 v7, v7, v15
	s_lshl_b64 s[26:27], s[30:31], 1
	v_pk_max_f16 v7, v7, 0
	v_pk_max_f16 v6, v6, 0
	v_pk_max_f16 v5, v5, 0
	v_pk_max_f16 v4, v4, 0
	ds_write_b128 v175, v[0:3] offset:32768
	ds_write_b128 v175, v[4:7] offset:40960
	s_add_u32 s26, s10, s26
	s_addc_u32 s27, s11, s27
	global_load_dwordx4 v[8:11], v168, s[24:25]
	s_add_u32 s26, s26, 0x80
	global_load_dwordx4 v[0:3], v170, s[24:25]
	s_addc_u32 s27, s27, 0
	global_load_dwordx4 v[12:15], v169, s[26:27]
	global_load_dwordx4 v[4:7], v171, s[26:27]
	s_waitcnt lgkmcnt(2)
	s_barrier
	s_waitcnt lgkmcnt(0)
	s_setprio 1
	s_waitcnt lgkmcnt(0)
	v_mfma_f32_16x16x32_f16 v[76:79], v[144:147], v[180:183], v[76:79]
	v_mfma_f32_16x16x32_f16 v[72:75], v[152:155], v[180:183], v[72:75]
	v_mfma_f32_16x16x32_f16 v[60:63], v[144:147], v[188:191], v[60:63]
	v_mfma_f32_16x16x32_f16 v[56:59], v[152:155], v[188:191], v[56:59]
	v_mfma_f32_16x16x32_f16 v[44:47], v[144:147], v[196:199], v[44:47]
	v_mfma_f32_16x16x32_f16 v[40:43], v[152:155], v[196:199], v[40:43]
	v_mfma_f32_16x16x32_f16 v[28:31], v[144:147], v[204:207], v[28:31]
	v_mfma_f32_16x16x32_f16 v[24:27], v[152:155], v[204:207], v[24:27]
	v_mfma_f32_16x16x32_f16 v[76:79], v[148:151], v[184:187], v[76:79]
	v_mfma_f32_16x16x32_f16 v[72:75], v[156:159], v[184:187], v[72:75]
	v_mfma_f32_16x16x32_f16 v[60:63], v[148:151], v[192:195], v[60:63]
	v_mfma_f32_16x16x32_f16 v[56:59], v[156:159], v[192:195], v[56:59]
	v_mfma_f32_16x16x32_f16 v[44:47], v[148:151], v[200:203], v[44:47]
	v_mfma_f32_16x16x32_f16 v[40:43], v[156:159], v[200:203], v[40:43]
	v_mfma_f32_16x16x32_f16 v[28:31], v[148:151], v[208:211], v[28:31]
	v_mfma_f32_16x16x32_f16 v[24:27], v[156:159], v[208:211], v[24:27]
	s_setprio 0
	s_setprio 1
	v_mfma_f32_16x16x32_f16 v[68:71], v[212:215], v[180:183], v[68:71]
	v_mfma_f32_16x16x32_f16 v[64:67], v[220:223], v[180:183], v[64:67]
	v_mfma_f32_16x16x32_f16 v[52:55], v[212:215], v[188:191], v[52:55]
	v_mfma_f32_16x16x32_f16 v[48:51], v[220:223], v[188:191], v[48:51]
	v_mfma_f32_16x16x32_f16 v[36:39], v[212:215], v[196:199], v[36:39]
	v_mfma_f32_16x16x32_f16 v[32:35], v[220:223], v[196:199], v[32:35]
	v_mfma_f32_16x16x32_f16 v[20:23], v[212:215], v[204:207], v[20:23]
	v_mfma_f32_16x16x32_f16 v[16:19], v[220:223], v[204:207], v[16:19]
	v_mfma_f32_16x16x32_f16 v[68:71], v[216:219], v[184:187], v[68:71]
	v_mfma_f32_16x16x32_f16 v[64:67], v[224:227], v[184:187], v[64:67]
	v_mfma_f32_16x16x32_f16 v[52:55], v[216:219], v[192:195], v[52:55]
	v_mfma_f32_16x16x32_f16 v[48:51], v[224:227], v[192:195], v[48:51]
	v_mfma_f32_16x16x32_f16 v[36:39], v[216:219], v[200:203], v[36:39]
	v_mfma_f32_16x16x32_f16 v[32:35], v[224:227], v[200:203], v[32:35]
	v_mfma_f32_16x16x32_f16 v[20:23], v[216:219], v[208:211], v[20:23]
	v_mfma_f32_16x16x32_f16 v[16:19], v[224:227], v[208:211], v[16:19]
	s_setprio 0
	s_add_i32 s24, s61, 2
	s_add_u32 s59, s59, 0x100
	s_addc_u32 s60, s60, 0
	s_cmp_ge_i32 s61, s49
	s_mov_b32 s61, s24
	s_barrier
	s_cbranch_scc0 .LBB8_37
	s_branch .LBB8_45
